# v57 + two 4-byte pads so the MFMA streams of the three GEMM K-loops sit on 8-byte boundaries again (code placement, microarch note 8)
# baseline (speedup 1.0000x reference)
.LBB0_264:
	s_ashr_i32 s73, s72, 31
	s_lshl_b64 s[26:27], s[72:73], 21
	s_add_u32 s76, s38, s26
	s_addc_u32 s77, s40, s27
	s_and_b64 s[26:27], s[4:5], exec
	s_cselect_b32 s73, s77, s7
	s_cselect_b32 vcc_lo, s76, s6
	s_ashr_i32 s75, s74, 31
	s_lshl_b64 s[26:27], s[74:75], 21
	s_add_u32 s96, s42, s26
	s_addc_u32 s97, s44, s27
	s_and_b64 s[26:27], s[4:5], exec
	s_cselect_b32 s75, s97, s25
	s_cselect_b32 vcc_hi, s96, s24
	s_add_u32 s6, s6, 0x100080
	s_addc_u32 s7, s7, 0
	s_add_u32 s21, s24, 0x100
	s_addc_u32 s13, s25, 0
	s_mov_b32 s58, -2
	s_nop 0
	s_add_u32 s24, s6, 0xfff00080
	s_addc_u32 s25, s7, -1
	s_add_i32 s28, 0, 0x10000
	s_cmp_eq_u32 s58, 60
	s_cselect_b32 s27, s73, s25
	s_cselect_b32 s26, vcc_lo, s24
	s_cselect_b32 s25, s75, s13
	s_cselect_b32 s24, vcc_hi, s21
	s_add_i32 s71, 0, 0x14000
	v_add_u32_e32 v144, s28, v163
	v_add_u32_e32 v182, s71, v163
	s_waitcnt lgkmcnt(0)
	ds_read_b128 v[132:135], v144
	ds_read_b128 v[136:139], v144 offset:1024
	ds_read_b128 v[140:143], v144 offset:2048
	ds_read_b128 v[144:147], v144 offset:3072
	ds_read_b128 v[148:151], v182
	ds_read_b128 v[152:155], v182 offset:1024
	ds_read_b128 v[178:181], v182 offset:2048
	ds_read_b128 v[186:189], v182 offset:3072
	v_lshl_add_u64 v[182:183], s[6:7], 0, v[174:175]
	s_add_i32 m0, s46, 0xc000
	ds_read_b128 v[190:193], v184
	ds_read_b128 v[194:197], v184 offset:1024
	ds_read_b128 v[198:201], v184 offset:2048
	ds_read_b128 v[202:205], v184 offset:3072
	ds_read_b128 v[222:225], v184 offset:4096
	ds_read_b128 v[226:229], v184 offset:5120
	ds_read_b128 v[230:233], v184 offset:6144
	ds_read_b128 v[234:237], v184 offset:7168
	global_load_lds_dwordx4 v[182:183], off
	v_lshl_add_u64 v[182:183], s[6:7], 0, v[176:177]
	s_add_i32 m0, s46, 0xe000
	s_nop 0
	global_load_lds_dwordx4 v[182:183], off
	s_waitcnt vmcnt(8)
	s_waitcnt lgkmcnt(0)
	s_setprio 1
	s_barrier
	v_mfma_f32_16x16x32_bf16 v[120:123], v[132:135], v[190:193], 0
	v_mfma_f32_16x16x32_bf16 v[116:119], v[140:143], v[190:193], 0
	v_mfma_f32_16x16x32_bf16 v[104:107], v[132:135], v[198:201], 0
	v_mfma_f32_16x16x32_bf16 v[100:103], v[140:143], v[198:201], 0
	v_mfma_f32_16x16x32_bf16 v[88:91], v[132:135], v[222:225], 0
	v_mfma_f32_16x16x32_bf16 v[84:87], v[140:143], v[222:225], 0
	v_mfma_f32_16x16x32_bf16 v[72:75], v[132:135], v[230:233], 0
	v_mfma_f32_16x16x32_bf16 v[68:71], v[140:143], v[230:233], 0
	v_mfma_f32_16x16x32_bf16 v[120:123], v[136:139], v[194:197], v[120:123]
	v_mfma_f32_16x16x32_bf16 v[116:119], v[144:147], v[194:197], v[116:119]
	v_mfma_f32_16x16x32_bf16 v[104:107], v[136:139], v[202:205], v[104:107]
	v_mfma_f32_16x16x32_bf16 v[100:103], v[144:147], v[202:205], v[100:103]
	v_mfma_f32_16x16x32_bf16 v[88:91], v[136:139], v[226:229], v[88:91]
	v_mfma_f32_16x16x32_bf16 v[84:87], v[144:147], v[226:229], v[84:87]
	v_mfma_f32_16x16x32_bf16 v[72:75], v[136:139], v[234:237], v[72:75]
	v_mfma_f32_16x16x32_bf16 v[68:71], v[144:147], v[234:237], v[68:71]
	v_mfma_f32_16x16x32_bf16 v[128:131], v[148:151], v[190:193], 0
	v_mfma_f32_16x16x32_bf16 v[124:127], v[178:181], v[190:193], 0
	v_mfma_f32_16x16x32_bf16 v[112:115], v[148:151], v[198:201], 0
	v_mfma_f32_16x16x32_bf16 v[108:111], v[178:181], v[198:201], 0
	v_mfma_f32_16x16x32_bf16 v[96:99], v[148:151], v[222:225], 0
	v_mfma_f32_16x16x32_bf16 v[92:95], v[178:181], v[222:225], 0
	v_mfma_f32_16x16x32_bf16 v[80:83], v[148:151], v[230:233], 0
	v_mfma_f32_16x16x32_bf16 v[76:79], v[178:181], v[230:233], 0
	v_mfma_f32_16x16x32_bf16 v[128:131], v[152:155], v[194:197], v[128:131]
	v_mfma_f32_16x16x32_bf16 v[124:127], v[186:189], v[194:197], v[124:127]
	v_mfma_f32_16x16x32_bf16 v[112:115], v[152:155], v[202:205], v[112:115]
	v_mfma_f32_16x16x32_bf16 v[108:111], v[186:189], v[202:205], v[108:111]
	v_mfma_f32_16x16x32_bf16 v[96:99], v[152:155], v[226:229], v[96:99]
	v_mfma_f32_16x16x32_bf16 v[92:95], v[186:189], v[226:229], v[92:95]
	v_mfma_f32_16x16x32_bf16 v[80:83], v[152:155], v[234:237], v[80:83]
	v_mfma_f32_16x16x32_bf16 v[76:79], v[186:189], v[234:237], v[76:79]
	s_barrier
	s_setprio 0
	s_add_i32 s28, s28, s1
	v_lshl_add_u64 v[182:183], s[24:25], 0, v[2:3]
	s_mov_b32 m0, s28
	ds_read_b128 v[190:193], v184 offset:16384
	ds_read_b128 v[194:197], v184 offset:17408
	ds_read_b128 v[198:201], v184 offset:18432
	ds_read_b128 v[202:205], v184 offset:19456
	ds_read_b128 v[222:225], v184 offset:20480
	ds_read_b128 v[226:229], v184 offset:21504
	ds_read_b128 v[230:233], v184 offset:22528
	ds_read_b128 v[234:237], v184 offset:23552
	global_load_lds_dwordx4 v[182:183], off
	s_add_i32 m0, s28, 0x2000
	s_add_u32 s28, s24, 0x100000
	v_lshl_add_u64 v[238:239], s[24:25], 0, v[168:169]
	s_addc_u32 s29, s25, 0
	s_add_i32 s71, s71, s1
	global_load_lds_dwordx4 v[238:239], off
	v_lshl_add_u64 v[240:241], s[28:29], 0, v[2:3]
	s_mov_b32 m0, s71
	v_lshl_add_u64 v[242:243], s[26:27], 0, v[170:171]
	global_load_lds_dwordx4 v[240:241], off
	v_lshl_add_u64 v[240:241], s[28:29], 0, v[168:169]
	s_add_i32 m0, s71, 0x2000
	s_nop 0
	global_load_lds_dwordx4 v[240:241], off
	v_lshl_add_u64 v[240:241], s[26:27], 0, v[172:173]
	s_mov_b32 m0, s46
	s_nop 0
	global_load_lds_dwordx4 v[240:241], off
	s_mov_b32 m0, s50
	s_nop 0
	global_load_lds_dwordx4 v[242:243], off
	s_waitcnt vmcnt(8)
	s_waitcnt lgkmcnt(0)
	s_setprio 1
	s_barrier
	v_mfma_f32_16x16x32_bf16 v[56:59], v[132:135], v[190:193], 0
	v_mfma_f32_16x16x32_bf16 v[52:55], v[140:143], v[190:193], 0
	v_mfma_f32_16x16x32_bf16 v[40:43], v[132:135], v[198:201], 0
	v_mfma_f32_16x16x32_bf16 v[36:39], v[140:143], v[198:201], 0
	v_mfma_f32_16x16x32_bf16 v[24:27], v[132:135], v[222:225], 0
	v_mfma_f32_16x16x32_bf16 v[20:23], v[140:143], v[222:225], 0
	v_mfma_f32_16x16x32_bf16 v[8:11], v[132:135], v[230:233], 0
	v_mfma_f32_16x16x32_bf16 v[4:7], v[140:143], v[230:233], 0
	v_mfma_f32_16x16x32_bf16 v[56:59], v[136:139], v[194:197], v[56:59]
	v_mfma_f32_16x16x32_bf16 v[52:55], v[144:147], v[194:197], v[52:55]
	v_mfma_f32_16x16x32_bf16 v[40:43], v[136:139], v[202:205], v[40:43]
	v_mfma_f32_16x16x32_bf16 v[36:39], v[144:147], v[202:205], v[36:39]
	v_mfma_f32_16x16x32_bf16 v[24:27], v[136:139], v[226:229], v[24:27]
	v_mfma_f32_16x16x32_bf16 v[20:23], v[144:147], v[226:229], v[20:23]
	v_mfma_f32_16x16x32_bf16 v[8:11], v[136:139], v[234:237], v[8:11]
	v_mfma_f32_16x16x32_bf16 v[4:7], v[144:147], v[234:237], v[4:7]
	v_mfma_f32_16x16x32_bf16 v[64:67], v[148:151], v[190:193], 0
	v_mfma_f32_16x16x32_bf16 v[60:63], v[178:181], v[190:193], 0
	v_mfma_f32_16x16x32_bf16 v[48:51], v[148:151], v[198:201], 0
	v_mfma_f32_16x16x32_bf16 v[44:47], v[178:181], v[198:201], 0
	v_mfma_f32_16x16x32_bf16 v[32:35], v[148:151], v[222:225], 0
	v_mfma_f32_16x16x32_bf16 v[28:31], v[178:181], v[222:225], 0
	v_mfma_f32_16x16x32_bf16 v[16:19], v[148:151], v[230:233], 0
	v_mfma_f32_16x16x32_bf16 v[12:15], v[178:181], v[230:233], 0
	v_mfma_f32_16x16x32_bf16 v[64:67], v[152:155], v[194:197], v[64:67]
	v_mfma_f32_16x16x32_bf16 v[60:63], v[186:189], v[194:197], v[60:63]
	v_mfma_f32_16x16x32_bf16 v[48:51], v[152:155], v[202:205], v[48:51]
	v_mfma_f32_16x16x32_bf16 v[44:47], v[186:189], v[202:205], v[44:47]
	v_mfma_f32_16x16x32_bf16 v[32:35], v[152:155], v[226:229], v[32:35]
	v_mfma_f32_16x16x32_bf16 v[28:31], v[186:189], v[226:229], v[28:31]
	v_mfma_f32_16x16x32_bf16 v[16:19], v[152:155], v[234:237], v[16:19]
	v_mfma_f32_16x16x32_bf16 v[12:15], v[186:189], v[234:237], v[12:15]
	s_barrier
	s_setprio 0
	s_add_i32 s28, 0, 0x18000
	s_add_i32 s29, 0, 0x1c000
	v_add_u32_e32 v144, s28, v163
	v_add_u32_e32 v185, s29, v163
	ds_read_b128 v[132:135], v144
	ds_read_b128 v[136:139], v144 offset:1024
	ds_read_b128 v[140:143], v144 offset:2048
	ds_read_b128 v[144:147], v144 offset:3072
	ds_read_b128 v[148:151], v185
	ds_read_b128 v[152:155], v185 offset:1024
	ds_read_b128 v[178:181], v185 offset:2048
	ds_read_b128 v[186:189], v185 offset:3072
	s_add_u32 s26, s26, 0x100000
	s_addc_u32 s27, s27, 0
	s_mov_b32 m0, s51
	v_lshl_add_u64 v[244:245], s[26:27], 0, v[172:173]
	ds_read_b128 v[190:193], v184 offset:32768
	ds_read_b128 v[194:197], v184 offset:33792
	ds_read_b128 v[198:201], v184 offset:34816
	ds_read_b128 v[202:205], v184 offset:35840
	ds_read_b128 v[222:225], v184 offset:36864
	ds_read_b128 v[226:229], v184 offset:37888
	ds_read_b128 v[230:233], v184 offset:38912
	ds_read_b128 v[234:237], v184 offset:39936
	global_load_lds_dwordx4 v[244:245], off
	v_lshl_add_u64 v[244:245], s[26:27], 0, v[170:171]
	s_mov_b32 m0, s54
	s_nop 0
	global_load_lds_dwordx4 v[244:245], off
	s_waitcnt vmcnt(8)
	s_waitcnt lgkmcnt(0)
	s_setprio 1
	s_barrier
	v_mfma_f32_16x16x32_bf16 v[120:123], v[132:135], v[190:193], v[120:123]
	v_mfma_f32_16x16x32_bf16 v[116:119], v[140:143], v[190:193], v[116:119]
	v_mfma_f32_16x16x32_bf16 v[104:107], v[132:135], v[198:201], v[104:107]
	v_mfma_f32_16x16x32_bf16 v[100:103], v[140:143], v[198:201], v[100:103]
	v_mfma_f32_16x16x32_bf16 v[88:91], v[132:135], v[222:225], v[88:91]
	v_mfma_f32_16x16x32_bf16 v[84:87], v[140:143], v[222:225], v[84:87]
	v_mfma_f32_16x16x32_bf16 v[72:75], v[132:135], v[230:233], v[72:75]
	v_mfma_f32_16x16x32_bf16 v[68:71], v[140:143], v[230:233], v[68:71]
	v_mfma_f32_16x16x32_bf16 v[120:123], v[136:139], v[194:197], v[120:123]
	v_mfma_f32_16x16x32_bf16 v[116:119], v[144:147], v[194:197], v[116:119]
	v_mfma_f32_16x16x32_bf16 v[104:107], v[136:139], v[202:205], v[104:107]
	v_mfma_f32_16x16x32_bf16 v[100:103], v[144:147], v[202:205], v[100:103]
	v_mfma_f32_16x16x32_bf16 v[88:91], v[136:139], v[226:229], v[88:91]
	v_mfma_f32_16x16x32_bf16 v[84:87], v[144:147], v[226:229], v[84:87]
	v_mfma_f32_16x16x32_bf16 v[72:75], v[136:139], v[234:237], v[72:75]
	v_mfma_f32_16x16x32_bf16 v[68:71], v[144:147], v[234:237], v[68:71]
	v_mfma_f32_16x16x32_bf16 v[128:131], v[148:151], v[190:193], v[128:131]
	v_mfma_f32_16x16x32_bf16 v[124:127], v[178:181], v[190:193], v[124:127]
	v_mfma_f32_16x16x32_bf16 v[112:115], v[148:151], v[198:201], v[112:115]
	v_mfma_f32_16x16x32_bf16 v[108:111], v[178:181], v[198:201], v[108:111]
	v_mfma_f32_16x16x32_bf16 v[96:99], v[148:151], v[222:225], v[96:99]
	v_mfma_f32_16x16x32_bf16 v[92:95], v[178:181], v[222:225], v[92:95]
	v_mfma_f32_16x16x32_bf16 v[80:83], v[148:151], v[230:233], v[80:83]
	v_mfma_f32_16x16x32_bf16 v[76:79], v[178:181], v[230:233], v[76:79]
	v_mfma_f32_16x16x32_bf16 v[128:131], v[152:155], v[194:197], v[128:131]
	v_mfma_f32_16x16x32_bf16 v[124:127], v[186:189], v[194:197], v[124:127]
	v_mfma_f32_16x16x32_bf16 v[112:115], v[152:155], v[202:205], v[112:115]
	v_mfma_f32_16x16x32_bf16 v[108:111], v[186:189], v[202:205], v[108:111]
	v_mfma_f32_16x16x32_bf16 v[96:99], v[152:155], v[226:229], v[96:99]
	v_mfma_f32_16x16x32_bf16 v[92:95], v[186:189], v[226:229], v[92:95]
	v_mfma_f32_16x16x32_bf16 v[80:83], v[152:155], v[234:237], v[80:83]
	v_mfma_f32_16x16x32_bf16 v[76:79], v[186:189], v[234:237], v[76:79]
	s_barrier
	s_setprio 0
	s_add_i32 s26, s28, s1
	v_lshl_add_u64 v[182:183], v[182:183], 0, s[86:87]
	s_mov_b32 m0, s26
	ds_read_b128 v[190:193], v184 offset:49152
	ds_read_b128 v[194:197], v184 offset:50176
	ds_read_b128 v[198:201], v184 offset:51200
	ds_read_b128 v[202:205], v184 offset:52224
	ds_read_b128 v[222:225], v184 offset:53248
	ds_read_b128 v[226:229], v184 offset:54272
	ds_read_b128 v[230:233], v184 offset:55296
	ds_read_b128 v[234:237], v184 offset:56320
	global_load_lds_dwordx4 v[182:183], off
	s_add_i32 m0, s26, 0x2000
	s_add_u32 s24, s24, 0x100080
	v_lshl_add_u64 v[182:183], v[238:239], 0, s[86:87]
	s_addc_u32 s25, s25, 0
	s_add_i32 s26, s29, s1
	global_load_lds_dwordx4 v[182:183], off
	v_lshl_add_u64 v[182:183], s[24:25], 0, v[2:3]
	s_mov_b32 m0, s26
	s_nop 0
	global_load_lds_dwordx4 v[182:183], off
	v_lshl_add_u64 v[182:183], s[24:25], 0, v[168:169]
	s_add_i32 m0, s26, 0x2000
	s_nop 0
	global_load_lds_dwordx4 v[182:183], off
	v_lshl_add_u64 v[182:183], v[240:241], 0, s[86:87]
	s_mov_b32 m0, s78
	s_nop 0
	global_load_lds_dwordx4 v[182:183], off
	v_lshl_add_u64 v[182:183], v[242:243], 0, s[86:87]
	s_mov_b32 m0, s85
	s_nop 0
	global_load_lds_dwordx4 v[182:183], off
	s_waitcnt vmcnt(8)
	s_waitcnt lgkmcnt(0)
	s_setprio 1
	s_barrier
	v_mfma_f32_16x16x32_bf16 v[56:59], v[132:135], v[190:193], v[56:59]
	v_mfma_f32_16x16x32_bf16 v[52:55], v[140:143], v[190:193], v[52:55]
	v_mfma_f32_16x16x32_bf16 v[40:43], v[132:135], v[198:201], v[40:43]
	v_mfma_f32_16x16x32_bf16 v[36:39], v[140:143], v[198:201], v[36:39]
	v_mfma_f32_16x16x32_bf16 v[24:27], v[132:135], v[222:225], v[24:27]
	v_mfma_f32_16x16x32_bf16 v[20:23], v[140:143], v[222:225], v[20:23]
	v_mfma_f32_16x16x32_bf16 v[8:11], v[132:135], v[230:233], v[8:11]
	v_mfma_f32_16x16x32_bf16 v[4:7], v[140:143], v[230:233], v[4:7]
	v_mfma_f32_16x16x32_bf16 v[56:59], v[136:139], v[194:197], v[56:59]
	v_mfma_f32_16x16x32_bf16 v[52:55], v[144:147], v[194:197], v[52:55]
	v_mfma_f32_16x16x32_bf16 v[40:43], v[136:139], v[202:205], v[40:43]
	v_mfma_f32_16x16x32_bf16 v[36:39], v[144:147], v[202:205], v[36:39]
	v_mfma_f32_16x16x32_bf16 v[24:27], v[136:139], v[226:229], v[24:27]
	v_mfma_f32_16x16x32_bf16 v[20:23], v[144:147], v[226:229], v[20:23]
	v_mfma_f32_16x16x32_bf16 v[8:11], v[136:139], v[234:237], v[8:11]
	v_mfma_f32_16x16x32_bf16 v[4:7], v[144:147], v[234:237], v[4:7]
	v_mfma_f32_16x16x32_bf16 v[64:67], v[148:151], v[190:193], v[64:67]
	v_mfma_f32_16x16x32_bf16 v[60:63], v[178:181], v[190:193], v[60:63]
	v_mfma_f32_16x16x32_bf16 v[48:51], v[148:151], v[198:201], v[48:51]
	v_mfma_f32_16x16x32_bf16 v[44:47], v[178:181], v[198:201], v[44:47]
	v_mfma_f32_16x16x32_bf16 v[32:35], v[148:151], v[222:225], v[32:35]
	v_mfma_f32_16x16x32_bf16 v[28:31], v[178:181], v[222:225], v[28:31]
	v_mfma_f32_16x16x32_bf16 v[16:19], v[148:151], v[230:233], v[16:19]
	v_mfma_f32_16x16x32_bf16 v[12:15], v[178:181], v[230:233], v[12:15]
	v_mfma_f32_16x16x32_bf16 v[64:67], v[152:155], v[194:197], v[64:67]
	v_mfma_f32_16x16x32_bf16 v[60:63], v[186:189], v[194:197], v[60:63]
	v_mfma_f32_16x16x32_bf16 v[48:51], v[152:155], v[202:205], v[48:51]
	v_mfma_f32_16x16x32_bf16 v[44:47], v[186:189], v[202:205], v[44:47]
	v_mfma_f32_16x16x32_bf16 v[32:35], v[152:155], v[226:229], v[32:35]
	v_mfma_f32_16x16x32_bf16 v[28:31], v[186:189], v[226:229], v[28:31]
	v_mfma_f32_16x16x32_bf16 v[16:19], v[152:155], v[234:237], v[16:19]
	v_mfma_f32_16x16x32_bf16 v[12:15], v[186:189], v[234:237], v[12:15]
	s_barrier
	s_setprio 0
	s_add_i32 s58, s58, 2
	s_add_u32 s6, s6, 0x100
	s_addc_u32 s7, s7, 0
	s_add_u32 s21, s21, 0x100
	s_addc_u32 s13, s13, 0
	s_cmp_gt_u32 s58, 61
	s_cbranch_scc0 .LBB0_265

.LBB0_1201:
	s_ashr_i32 s53, s52, 31
	s_lshl_b64 s[26:27], s[52:53], 21
	s_add_u32 s72, s38, s26
	s_addc_u32 s73, s40, s27
	s_and_b64 s[26:27], s[4:5], exec
	s_cselect_b32 s35, s73, s7
	s_cselect_b32 s53, s72, s6
	s_ashr_i32 s31, s30, 31
	s_lshl_b64 s[26:27], s[30:31], 21
	s_add_u32 s74, s42, s26
	s_addc_u32 s75, s44, s27
	s_and_b64 s[26:27], s[4:5], exec
	s_cselect_b32 s31, s75, s25
	s_cselect_b32 s92, s74, s24
	s_add_u32 s6, s6, 0x100080
	s_addc_u32 s7, s7, 0
	s_add_u32 s21, s24, 0x100
	s_addc_u32 s13, s25, 0
	s_mov_b32 s58, -2
	s_waitcnt lgkmcnt(0)
	s_add_u32 s24, s6, 0xfff00080
	s_addc_u32 s25, s7, -1
	s_add_i32 s28, 0, 0x10000
	s_cmp_eq_u32 s58, 60
	s_cselect_b32 s27, s35, s25
	s_cselect_b32 s26, s53, s24
	s_cselect_b32 s25, s31, s13
	s_cselect_b32 s24, s92, s21
	s_add_i32 s71, 0, 0x14000
	v_add_u32_e32 v150, s28, v163
	v_add_u32_e32 v154, s71, v163
	ds_read_b128 v[138:141], v150
	ds_read_b128 v[142:145], v150 offset:1024
	ds_read_b128 v[146:149], v150 offset:2048
	ds_read_b128 v[150:153], v150 offset:3072
	ds_read_b128 v[168:171], v154
	ds_read_b128 v[172:175], v154 offset:1024
	ds_read_b128 v[176:179], v154 offset:2048
	ds_read_b128 v[180:183], v154 offset:3072
	v_lshl_add_u64 v[154:155], s[6:7], 0, v[134:135]
	s_add_i32 m0, s50, 0xc000
	ds_read_b128 v[188:191], v186
	ds_read_b128 v[192:195], v186 offset:1024
	ds_read_b128 v[196:199], v186 offset:2048
	ds_read_b128 v[200:203], v186 offset:3072
	ds_read_b128 v[222:225], v186 offset:4096
	ds_read_b128 v[226:229], v186 offset:5120
	ds_read_b128 v[230:233], v186 offset:6144
	ds_read_b128 v[234:237], v186 offset:7168
	global_load_lds_dwordx4 v[154:155], off
	v_lshl_add_u64 v[154:155], s[6:7], 0, v[136:137]
	s_add_i32 m0, s50, 0xe000
	s_nop 0
	global_load_lds_dwordx4 v[154:155], off
	s_waitcnt vmcnt(8)
	s_waitcnt lgkmcnt(0)
	s_setprio 1
	s_barrier
	v_mfma_f32_16x16x32_bf16 v[128:131], v[138:141], v[188:191], 0
	v_mfma_f32_16x16x32_bf16 v[124:127], v[146:149], v[188:191], 0
	v_mfma_f32_16x16x32_bf16 v[112:115], v[138:141], v[196:199], 0
	v_mfma_f32_16x16x32_bf16 v[108:111], v[146:149], v[196:199], 0
	v_mfma_f32_16x16x32_bf16 v[96:99], v[138:141], v[222:225], 0
	v_mfma_f32_16x16x32_bf16 v[92:95], v[146:149], v[222:225], 0
	v_mfma_f32_16x16x32_bf16 v[80:83], v[138:141], v[230:233], 0
	v_mfma_f32_16x16x32_bf16 v[76:79], v[146:149], v[230:233], 0
	v_mfma_f32_16x16x32_bf16 v[128:131], v[142:145], v[192:195], v[128:131]
	v_mfma_f32_16x16x32_bf16 v[124:127], v[150:153], v[192:195], v[124:127]
	v_mfma_f32_16x16x32_bf16 v[112:115], v[142:145], v[200:203], v[112:115]
	v_mfma_f32_16x16x32_bf16 v[108:111], v[150:153], v[200:203], v[108:111]
	v_mfma_f32_16x16x32_bf16 v[96:99], v[142:145], v[226:229], v[96:99]
	v_mfma_f32_16x16x32_bf16 v[92:95], v[150:153], v[226:229], v[92:95]
	v_mfma_f32_16x16x32_bf16 v[80:83], v[142:145], v[234:237], v[80:83]
	v_mfma_f32_16x16x32_bf16 v[76:79], v[150:153], v[234:237], v[76:79]
	v_mfma_f32_16x16x32_bf16 v[120:123], v[168:171], v[188:191], 0
	v_mfma_f32_16x16x32_bf16 v[116:119], v[176:179], v[188:191], 0
	v_mfma_f32_16x16x32_bf16 v[104:107], v[168:171], v[196:199], 0
	v_mfma_f32_16x16x32_bf16 v[100:103], v[176:179], v[196:199], 0
	v_mfma_f32_16x16x32_bf16 v[88:91], v[168:171], v[222:225], 0
	v_mfma_f32_16x16x32_bf16 v[84:87], v[176:179], v[222:225], 0
	v_mfma_f32_16x16x32_bf16 v[72:75], v[168:171], v[230:233], 0
	v_mfma_f32_16x16x32_bf16 v[68:71], v[176:179], v[230:233], 0
	v_mfma_f32_16x16x32_bf16 v[120:123], v[172:175], v[192:195], v[120:123]
	v_mfma_f32_16x16x32_bf16 v[116:119], v[180:183], v[192:195], v[116:119]
	v_mfma_f32_16x16x32_bf16 v[104:107], v[172:175], v[200:203], v[104:107]
	v_mfma_f32_16x16x32_bf16 v[100:103], v[180:183], v[200:203], v[100:103]
	v_mfma_f32_16x16x32_bf16 v[88:91], v[172:175], v[226:229], v[88:91]
	v_mfma_f32_16x16x32_bf16 v[84:87], v[180:183], v[226:229], v[84:87]
	v_mfma_f32_16x16x32_bf16 v[72:75], v[172:175], v[234:237], v[72:75]
	v_mfma_f32_16x16x32_bf16 v[68:71], v[180:183], v[234:237], v[68:71]
	s_barrier
	s_setprio 0
	s_add_i32 s28, s28, s46
	v_lshl_add_u64 v[154:155], s[24:25], 0, v[2:3]
	s_mov_b32 m0, s28
	ds_read_b128 v[188:191], v186 offset:16384
	ds_read_b128 v[192:195], v186 offset:17408
	ds_read_b128 v[196:199], v186 offset:18432
	ds_read_b128 v[200:203], v186 offset:19456
	ds_read_b128 v[222:225], v186 offset:20480
	ds_read_b128 v[226:229], v186 offset:21504
	ds_read_b128 v[230:233], v186 offset:22528
	ds_read_b128 v[234:237], v186 offset:23552
	global_load_lds_dwordx4 v[154:155], off
	s_add_i32 m0, s28, 0x2000
	s_add_u32 s28, s24, 0x100000
	v_lshl_add_u64 v[184:185], s[24:25], 0, v[132:133]
	s_addc_u32 s29, s25, 0
	s_add_i32 s71, s71, s46
	global_load_lds_dwordx4 v[184:185], off
	v_lshl_add_u64 v[204:205], s[28:29], 0, v[2:3]
	s_mov_b32 m0, s71
	v_lshl_add_u64 v[238:239], s[26:27], 0, v[132:133]
	global_load_lds_dwordx4 v[204:205], off
	v_lshl_add_u64 v[204:205], s[28:29], 0, v[132:133]
	s_add_i32 m0, s71, 0x2000
	s_nop 0
	global_load_lds_dwordx4 v[204:205], off
	v_lshl_add_u64 v[204:205], s[26:27], 0, v[2:3]
	s_mov_b32 m0, s50
	s_nop 0
	global_load_lds_dwordx4 v[204:205], off
	s_mov_b32 m0, s23
	s_nop 0
	global_load_lds_dwordx4 v[238:239], off
	s_waitcnt vmcnt(8)
	s_waitcnt lgkmcnt(0)
	s_setprio 1
	s_barrier
	v_mfma_f32_16x16x32_bf16 v[64:67], v[138:141], v[188:191], 0
	v_mfma_f32_16x16x32_bf16 v[60:63], v[146:149], v[188:191], 0
	v_mfma_f32_16x16x32_bf16 v[48:51], v[138:141], v[196:199], 0
	v_mfma_f32_16x16x32_bf16 v[44:47], v[146:149], v[196:199], 0
	v_mfma_f32_16x16x32_bf16 v[32:35], v[138:141], v[222:225], 0
	v_mfma_f32_16x16x32_bf16 v[28:31], v[146:149], v[222:225], 0
	v_mfma_f32_16x16x32_bf16 v[16:19], v[138:141], v[230:233], 0
	v_mfma_f32_16x16x32_bf16 v[12:15], v[146:149], v[230:233], 0
	v_mfma_f32_16x16x32_bf16 v[64:67], v[142:145], v[192:195], v[64:67]
	v_mfma_f32_16x16x32_bf16 v[60:63], v[150:153], v[192:195], v[60:63]
	v_mfma_f32_16x16x32_bf16 v[48:51], v[142:145], v[200:203], v[48:51]
	v_mfma_f32_16x16x32_bf16 v[44:47], v[150:153], v[200:203], v[44:47]
	v_mfma_f32_16x16x32_bf16 v[32:35], v[142:145], v[226:229], v[32:35]
	v_mfma_f32_16x16x32_bf16 v[28:31], v[150:153], v[226:229], v[28:31]
	v_mfma_f32_16x16x32_bf16 v[16:19], v[142:145], v[234:237], v[16:19]
	v_mfma_f32_16x16x32_bf16 v[12:15], v[150:153], v[234:237], v[12:15]
	v_mfma_f32_16x16x32_bf16 v[56:59], v[168:171], v[188:191], 0
	v_mfma_f32_16x16x32_bf16 v[52:55], v[176:179], v[188:191], 0
	v_mfma_f32_16x16x32_bf16 v[40:43], v[168:171], v[196:199], 0
	v_mfma_f32_16x16x32_bf16 v[36:39], v[176:179], v[196:199], 0
	v_mfma_f32_16x16x32_bf16 v[24:27], v[168:171], v[222:225], 0
	v_mfma_f32_16x16x32_bf16 v[20:23], v[176:179], v[222:225], 0
	v_mfma_f32_16x16x32_bf16 v[8:11], v[168:171], v[230:233], 0
	v_mfma_f32_16x16x32_bf16 v[4:7], v[176:179], v[230:233], 0
	v_mfma_f32_16x16x32_bf16 v[56:59], v[172:175], v[192:195], v[56:59]
	v_mfma_f32_16x16x32_bf16 v[52:55], v[180:183], v[192:195], v[52:55]
	v_mfma_f32_16x16x32_bf16 v[40:43], v[172:175], v[200:203], v[40:43]
	v_mfma_f32_16x16x32_bf16 v[36:39], v[180:183], v[200:203], v[36:39]
	v_mfma_f32_16x16x32_bf16 v[24:27], v[172:175], v[226:229], v[24:27]
	v_mfma_f32_16x16x32_bf16 v[20:23], v[180:183], v[226:229], v[20:23]
	v_mfma_f32_16x16x32_bf16 v[8:11], v[172:175], v[234:237], v[8:11]
	v_mfma_f32_16x16x32_bf16 v[4:7], v[180:183], v[234:237], v[4:7]
	s_barrier
	s_setprio 0
	s_add_i32 s28, 0, 0x18000
	s_add_i32 s29, 0, 0x1c000
	v_add_u32_e32 v150, s28, v163
	v_add_u32_e32 v180, s29, v163
	ds_read_b128 v[138:141], v150
	ds_read_b128 v[142:145], v150 offset:1024
	ds_read_b128 v[146:149], v150 offset:2048
	ds_read_b128 v[150:153], v150 offset:3072
	ds_read_b128 v[168:171], v180
	ds_read_b128 v[172:175], v180 offset:1024
	ds_read_b128 v[176:179], v180 offset:2048
	ds_read_b128 v[180:183], v180 offset:3072
	s_add_u32 s26, s26, 0x100000
	s_addc_u32 s27, s27, 0
	s_mov_b32 m0, s51
	v_lshl_add_u64 v[240:241], s[26:27], 0, v[2:3]
	ds_read_b128 v[188:191], v186 offset:32768
	ds_read_b128 v[192:195], v186 offset:33792
	ds_read_b128 v[196:199], v186 offset:34816
	ds_read_b128 v[200:203], v186 offset:35840
	ds_read_b128 v[222:225], v186 offset:36864
	ds_read_b128 v[226:229], v186 offset:37888
	ds_read_b128 v[230:233], v186 offset:38912
	ds_read_b128 v[234:237], v186 offset:39936
	global_load_lds_dwordx4 v[240:241], off
	v_lshl_add_u64 v[240:241], s[26:27], 0, v[132:133]
	s_mov_b32 m0, s54
	s_nop 0
	global_load_lds_dwordx4 v[240:241], off
	s_waitcnt vmcnt(8)
	s_waitcnt lgkmcnt(0)
	s_setprio 1
	s_barrier
	v_mfma_f32_16x16x32_bf16 v[128:131], v[138:141], v[188:191], v[128:131]
	v_mfma_f32_16x16x32_bf16 v[124:127], v[146:149], v[188:191], v[124:127]
	v_mfma_f32_16x16x32_bf16 v[112:115], v[138:141], v[196:199], v[112:115]
	v_mfma_f32_16x16x32_bf16 v[108:111], v[146:149], v[196:199], v[108:111]
	v_mfma_f32_16x16x32_bf16 v[96:99], v[138:141], v[222:225], v[96:99]
	v_mfma_f32_16x16x32_bf16 v[92:95], v[146:149], v[222:225], v[92:95]
	v_mfma_f32_16x16x32_bf16 v[80:83], v[138:141], v[230:233], v[80:83]
	v_mfma_f32_16x16x32_bf16 v[76:79], v[146:149], v[230:233], v[76:79]
	v_mfma_f32_16x16x32_bf16 v[128:131], v[142:145], v[192:195], v[128:131]
	v_mfma_f32_16x16x32_bf16 v[124:127], v[150:153], v[192:195], v[124:127]
	v_mfma_f32_16x16x32_bf16 v[112:115], v[142:145], v[200:203], v[112:115]
	v_mfma_f32_16x16x32_bf16 v[108:111], v[150:153], v[200:203], v[108:111]
	v_mfma_f32_16x16x32_bf16 v[96:99], v[142:145], v[226:229], v[96:99]
	v_mfma_f32_16x16x32_bf16 v[92:95], v[150:153], v[226:229], v[92:95]
	v_mfma_f32_16x16x32_bf16 v[80:83], v[142:145], v[234:237], v[80:83]
	v_mfma_f32_16x16x32_bf16 v[76:79], v[150:153], v[234:237], v[76:79]
	v_mfma_f32_16x16x32_bf16 v[120:123], v[168:171], v[188:191], v[120:123]
	v_mfma_f32_16x16x32_bf16 v[116:119], v[176:179], v[188:191], v[116:119]
	v_mfma_f32_16x16x32_bf16 v[104:107], v[168:171], v[196:199], v[104:107]
	v_mfma_f32_16x16x32_bf16 v[100:103], v[176:179], v[196:199], v[100:103]
	v_mfma_f32_16x16x32_bf16 v[88:91], v[168:171], v[222:225], v[88:91]
	v_mfma_f32_16x16x32_bf16 v[84:87], v[176:179], v[222:225], v[84:87]
	v_mfma_f32_16x16x32_bf16 v[72:75], v[168:171], v[230:233], v[72:75]
	v_mfma_f32_16x16x32_bf16 v[68:71], v[176:179], v[230:233], v[68:71]
	v_mfma_f32_16x16x32_bf16 v[120:123], v[172:175], v[192:195], v[120:123]
	v_mfma_f32_16x16x32_bf16 v[116:119], v[180:183], v[192:195], v[116:119]
	v_mfma_f32_16x16x32_bf16 v[104:107], v[172:175], v[200:203], v[104:107]
	v_mfma_f32_16x16x32_bf16 v[100:103], v[180:183], v[200:203], v[100:103]
	v_mfma_f32_16x16x32_bf16 v[88:91], v[172:175], v[226:229], v[88:91]
	v_mfma_f32_16x16x32_bf16 v[84:87], v[180:183], v[226:229], v[84:87]
	v_mfma_f32_16x16x32_bf16 v[72:75], v[172:175], v[234:237], v[72:75]
	v_mfma_f32_16x16x32_bf16 v[68:71], v[180:183], v[234:237], v[68:71]
	s_barrier
	s_setprio 0
	s_add_i32 s26, s28, s46
	v_lshl_add_u64 v[154:155], v[154:155], 0, s[86:87]
	s_mov_b32 m0, s26
	ds_read_b128 v[188:191], v186 offset:49152
	ds_read_b128 v[192:195], v186 offset:50176
	ds_read_b128 v[196:199], v186 offset:51200
	ds_read_b128 v[200:203], v186 offset:52224
	ds_read_b128 v[222:225], v186 offset:53248
	ds_read_b128 v[226:229], v186 offset:54272
	ds_read_b128 v[230:233], v186 offset:55296
	ds_read_b128 v[234:237], v186 offset:56320
	global_load_lds_dwordx4 v[154:155], off
	s_add_i32 m0, s26, 0x2000
	s_add_u32 s24, s24, 0x100080
	v_lshl_add_u64 v[154:155], v[184:185], 0, s[86:87]
	s_addc_u32 s25, s25, 0
	s_add_i32 s26, s29, s46
	global_load_lds_dwordx4 v[154:155], off
	v_lshl_add_u64 v[154:155], s[24:25], 0, v[2:3]
	s_mov_b32 m0, s26
	s_nop 0
	global_load_lds_dwordx4 v[154:155], off
	v_lshl_add_u64 v[154:155], s[24:25], 0, v[132:133]
	s_add_i32 m0, s26, 0x2000
	s_nop 0
	global_load_lds_dwordx4 v[154:155], off
	v_lshl_add_u64 v[154:155], v[204:205], 0, s[86:87]
	s_mov_b32 m0, s76
	s_nop 0
	global_load_lds_dwordx4 v[154:155], off
	v_lshl_add_u64 v[154:155], v[238:239], 0, s[86:87]
	s_mov_b32 m0, s77
	s_nop 0
	global_load_lds_dwordx4 v[154:155], off
	s_waitcnt vmcnt(8)
	s_waitcnt lgkmcnt(0)
	s_setprio 1
	s_barrier
	v_mfma_f32_16x16x32_bf16 v[64:67], v[138:141], v[188:191], v[64:67]
	v_mfma_f32_16x16x32_bf16 v[60:63], v[146:149], v[188:191], v[60:63]
	v_mfma_f32_16x16x32_bf16 v[48:51], v[138:141], v[196:199], v[48:51]
	v_mfma_f32_16x16x32_bf16 v[44:47], v[146:149], v[196:199], v[44:47]
	v_mfma_f32_16x16x32_bf16 v[32:35], v[138:141], v[222:225], v[32:35]
	v_mfma_f32_16x16x32_bf16 v[28:31], v[146:149], v[222:225], v[28:31]
	v_mfma_f32_16x16x32_bf16 v[16:19], v[138:141], v[230:233], v[16:19]
	v_mfma_f32_16x16x32_bf16 v[12:15], v[146:149], v[230:233], v[12:15]
	v_mfma_f32_16x16x32_bf16 v[64:67], v[142:145], v[192:195], v[64:67]
	v_mfma_f32_16x16x32_bf16 v[60:63], v[150:153], v[192:195], v[60:63]
	v_mfma_f32_16x16x32_bf16 v[48:51], v[142:145], v[200:203], v[48:51]
	v_mfma_f32_16x16x32_bf16 v[44:47], v[150:153], v[200:203], v[44:47]
	v_mfma_f32_16x16x32_bf16 v[32:35], v[142:145], v[226:229], v[32:35]
	v_mfma_f32_16x16x32_bf16 v[28:31], v[150:153], v[226:229], v[28:31]
	v_mfma_f32_16x16x32_bf16 v[16:19], v[142:145], v[234:237], v[16:19]
	v_mfma_f32_16x16x32_bf16 v[12:15], v[150:153], v[234:237], v[12:15]
	v_mfma_f32_16x16x32_bf16 v[56:59], v[168:171], v[188:191], v[56:59]
	v_mfma_f32_16x16x32_bf16 v[52:55], v[176:179], v[188:191], v[52:55]
	v_mfma_f32_16x16x32_bf16 v[40:43], v[168:171], v[196:199], v[40:43]
	v_mfma_f32_16x16x32_bf16 v[36:39], v[176:179], v[196:199], v[36:39]
	v_mfma_f32_16x16x32_bf16 v[24:27], v[168:171], v[222:225], v[24:27]
	v_mfma_f32_16x16x32_bf16 v[20:23], v[176:179], v[222:225], v[20:23]
	v_mfma_f32_16x16x32_bf16 v[8:11], v[168:171], v[230:233], v[8:11]
	v_mfma_f32_16x16x32_bf16 v[4:7], v[176:179], v[230:233], v[4:7]
	v_mfma_f32_16x16x32_bf16 v[56:59], v[172:175], v[192:195], v[56:59]
	v_mfma_f32_16x16x32_bf16 v[52:55], v[180:183], v[192:195], v[52:55]
	v_mfma_f32_16x16x32_bf16 v[40:43], v[172:175], v[200:203], v[40:43]
	v_mfma_f32_16x16x32_bf16 v[36:39], v[180:183], v[200:203], v[36:39]
	v_mfma_f32_16x16x32_bf16 v[24:27], v[172:175], v[226:229], v[24:27]
	v_mfma_f32_16x16x32_bf16 v[20:23], v[180:183], v[226:229], v[20:23]
	v_mfma_f32_16x16x32_bf16 v[8:11], v[172:175], v[234:237], v[8:11]
	v_mfma_f32_16x16x32_bf16 v[4:7], v[180:183], v[234:237], v[4:7]
	s_barrier
	s_setprio 0
	s_add_i32 s58, s58, 2
	s_add_u32 s6, s6, 0x100
	s_addc_u32 s7, s7, 0
	s_add_u32 s21, s21, 0x100
	s_addc_u32 s13, s13, 0
	s_cmp_gt_u32 s58, 61
	s_cbranch_scc0 .LBB0_1202
	s_nop 0
